# v55 with the moe_gu unit-head vmcnt(0) drain restored (the v50 change reverted; it was timing-neutral)
# baseline (speedup 1.0000x reference)
.LBB0_1553:
	s_add_u32 s22, s22, 0x80
	s_addc_u32 s23, s23, 0
	s_add_u32 s2, s24, 0x100
	v_mov_b32_e32 v169, v173
	v_mov_b32_e32 v175, v173
	s_addc_u32 s3, s25, 0
	s_mov_b32 s64, -2
	v_mov_b32_e32 v218, v2
	v_mov_b32_e32 v217, v4
	v_mov_b32_e32 v216, v3
	v_mov_b32_e32 v215, v1
	s_waitcnt vmcnt(0)
